# k_bscatter: non-temporal loads for the last-use edge arrays (src, dst, w)
# baseline (speedup 1.0000x reference)
.LBB0_100:
	s_or_b64 exec, exec, s[28:29]
	s_mul_i32 s28, s2, 0xf43
	s_min_i32 s29, s28, 0xf32fd
	s_addk_i32 s29, 0xf43
	v_add_u32_e32 v8, s28, v0
	v_cmp_gt_i32_e64 s[14:15], s29, v8
	v_mov_b32_e32 v22, -1
	v_ashrrev_i32_e32 v9, 31, v8
	s_waitcnt lgkmcnt(0)
	s_barrier
	s_and_saveexec_b64 s[2:3], s[14:15]
	s_cbranch_execz .LBB0_102
	v_lshl_add_u64 v[2:3], v[8:9], 2, s[16:17]
	global_load_dword v22, v[2:3], off nt
.LBB0_102:
	s_or_b64 exec, exec, s[2:3]
	v_mov_b32_e32 v2, 0
	v_mov_b32_e32 v7, 0
	s_and_saveexec_b64 s[2:3], s[14:15]
	s_cbranch_execz .LBB0_104
	v_lshlrev_b64 v[4:5], 2, v[8:9]
	v_lshl_add_u64 v[2:3], s[20:21], 0, v[4:5]
	v_lshl_add_u64 v[4:5], s[18:19], 0, v[4:5]
	global_load_dword v2, v[2:3], off nt
	s_nop 0
	global_load_dword v7, v[4:5], off nt
.LBB0_104:
	s_or_b64 exec, exec, s[2:3]
	v_add_u32_e32 v10, 0x400, v8
	v_cmp_le_i32_e64 s[14:15], s29, v10
	v_cmp_gt_i32_e64 s[2:3], s29, v10
	v_mov_b32_e32 v23, -1
	v_ashrrev_i32_e32 v11, 31, v10
	s_and_saveexec_b64 s[24:25], s[2:3]
	s_cbranch_execz .LBB0_106
	v_lshl_add_u64 v[4:5], v[10:11], 2, s[16:17]
	global_load_dword v23, v[4:5], off nt
.LBB0_106:
	s_or_b64 exec, exec, s[24:25]
	v_mov_b32_e32 v9, 0
	s_and_saveexec_b64 s[2:3], s[14:15]
	s_xor_b64 s[2:3], exec, s[2:3]
	s_mov_b32 s14, 0
	v_mov_b32_e32 v1, s14
	s_andn2_saveexec_b64 s[2:3], s[2:3]
	s_cbranch_execz .LBB0_110
	v_lshlrev_b64 v[10:11], 2, v[10:11]
	v_lshl_add_u64 v[12:13], s[20:21], 0, v[10:11]
	v_lshl_add_u64 v[10:11], s[18:19], 0, v[10:11]
	global_load_dword v1, v[12:13], off nt
	global_load_dword v9, v[10:11], off nt

.LBB0_113:
	v_lshlrev_b64 v[10:11], 2, v[10:11]
	v_lshl_add_u64 v[4:5], s[20:21], 0, v[10:11]
	v_lshl_add_u64 v[10:11], s[18:19], 0, v[10:11]
	global_load_dword v4, v[4:5], off nt
	s_nop 0
	global_load_dword v5, v[10:11], off nt
